# P0 RMSNorm: loop-invariant norm_mix gain loaded once at kernel start (v134-149) instead of 4 loads + full vmcnt(0) drains between output stores per 4-row item
# speedup vs baseline: 1.0004x; 1.0004x over previous
.Lplace_ok:
.LBB0_13:
	s_or_b64 exec, exec, s[0:1]
	s_add_u32 s72, s90, 0x100000
	s_addc_u32 s73, s91, 0
	s_add_u32 s70, s90, 0xe00000
	s_addc_u32 s71, s91, 0
	s_add_u32 s0, s90, 0xd800000
	s_addc_u32 s1, s91, 0
	s_add_u32 s74, s90, 0x200000
	v_writelane_b32 v255, s0, 14
	s_addc_u32 s75, s91, 0
	s_nop 0
	v_writelane_b32 v255, s1, 15
	s_add_u32 s0, s90, 0x1100000
	s_addc_u32 s1, s91, 0
	v_writelane_b32 v255, s0, 16
	s_nop 1
	v_writelane_b32 v255, s1, 17
	s_lshr_b32 s0, s10, 6
	v_readlane_b32 s5, v255, 2
	s_abs_i32 s94, s5
	v_cvt_f32_u32_e32 v1, s94
	s_sub_i32 s2, 0, s94
	v_writelane_b32 v255, s0, 18
	s_add_i32 s0, s5, 0xfff
	v_rcp_iflag_f32_e32 v1, v1
	s_ashr_i32 s1, s0, 31
	s_abs_i32 s0, s0
	s_ashr_i32 s6, s5, 31
	v_mul_f32_e32 v1, 0x4f7ffffe, v1
	v_cvt_u32_f32_e32 v1, v1
	s_xor_b32 s1, s1, s6
	v_writelane_b32 v255, s6, 19
	v_readfirstlane_b32 s3, v1
	s_mul_i32 s2, s2, s3
	s_mul_hi_u32 s2, s3, s2
	s_add_i32 s96, s3, s2
	s_mul_hi_u32 s2, s0, s96
	s_mul_i32 s3, s2, s94
	s_sub_i32 s0, s0, s3
	s_add_i32 s4, s2, 1
	s_sub_i32 s3, s0, s94
	s_cmp_ge_u32 s0, s94
	s_cselect_b32 s2, s4, s2
	s_cselect_b32 s0, s3, s0
	s_add_i32 s3, s2, 1
	s_cmp_ge_u32 s0, s94
	s_cselect_b32 s0, s3, s2
	s_xor_b32 s0, s0, s1
	s_sub_i32 s33, s0, s1
	s_add_i32 s0, s5, 0xbfff
	s_ashr_i32 s1, s0, 31
	s_abs_i32 s0, s0
	s_mul_hi_u32 s2, s0, s96
	s_mul_i32 s3, s2, s94
	s_sub_i32 s0, s0, s3
	s_xor_b32 s1, s1, s6
	s_add_i32 s3, s2, 1
	s_sub_i32 s4, s0, s94
	s_cmp_ge_u32 s0, s94
	s_cselect_b32 s2, s3, s2
	s_cselect_b32 s0, s4, s0
	s_add_i32 s3, s2, 1
	s_cmp_ge_u32 s0, s94
	s_cselect_b32 s0, s3, s2
	s_xor_b32 s0, s0, s1
	s_sub_i32 s0, s0, s1
	s_min_i32 s34, s0, 0
	s_add_i32 s34, s34, s33
	s_cmp_lt_i32 s80, 1
	v_writelane_b32 v255, s0, 20
	s_cselect_b64 s[0:1], -1, 0
	s_cmp_gt_i32 s81, 0
	s_cselect_b64 s[2:3], -1, 0
	v_writelane_b32 v255, s90, 21
	s_and_b64 s[68:69], s[0:1], s[2:3]
	s_mov_b64 s[0:1], s[80:81]
	v_writelane_b32 v255, s91, 22
	v_writelane_b32 v255, s0, 23
	s_andn2_b64 vcc, exec, s[68:69]
	v_and_b32_e32 v1, 63, v0
	v_writelane_b32 v255, s1, 24
	v_writelane_b32 v255, s2, 25
	v_writelane_b32 v255, s3, 26
	v_writelane_b32 v255, s10, 27
	s_cbranch_vccnz .LBB0_220
	v_readlane_b32 s0, v255, 2
	s_lshl_b32 s4, s0, 2
	s_abs_i32 s2, s4
	v_cvt_f32_u32_e32 v2, s2
	s_add_i32 s5, s4, 0x3fff
	s_abs_i32 s3, s5
	v_rcp_iflag_f32_e32 v3, v2
	s_sub_i32 s0, 0, s2
	v_mul_f32_e32 v3, 0x4f7ffffe, v3
	v_cvt_u32_f32_e32 v3, v3
	s_nop 0
	v_readfirstlane_b32 s6, v3
	s_mul_i32 s0, s0, s6
	s_mul_hi_u32 s0, s6, s0
	s_add_i32 s6, s6, s0
	s_mul_hi_u32 s6, s3, s6
	s_ashr_i32 s5, s5, 31
	s_ashr_i32 s4, s4, 31
	s_mov_b64 s[0:1], exec
	v_readlane_b32 s8, v255, 12
	v_readlane_b32 s9, v255, 13
	s_and_b64 s[8:9], s[0:1], s[8:9]
	s_mov_b64 exec, s[8:9]
	s_add_i32 s7, 0, 0x20280
	v_mov_b32_e32 v2, 0
	v_mov_b32_e32 v3, v2
	v_mov_b32_e32 v4, s7
	ds_write_b64 v4, v[2:3]
	s_or_b64 exec, exec, s[0:1]
	s_mul_i32 s1, s6, s2
	s_sub_i32 s1, s3, s1
	s_xor_b32 s0, s5, s4
	s_add_i32 s3, s6, 1
	s_sub_i32 s4, s1, s2
	s_cmp_ge_u32 s1, s2
	s_cselect_b32 s3, s3, s6
	s_cselect_b32 s1, s4, s1
	s_add_i32 s4, s3, 1
	s_cmp_ge_u32 s1, s2
	s_cselect_b32 s1, s4, s3
	s_xor_b32 s1, s1, s0
	s_sub_i32 s35, s1, s0
	s_cmp_gt_i32 s35, 0
	s_cselect_b64 s[76:77], -1, 0
	s_cmp_gt_i32 s34, 0
	s_cselect_b64 s[78:79], -1, 0
	s_or_b64 s[0:1], s[78:79], s[76:77]
	s_mov_b32 s23, 0
	s_andn2_b64 vcc, exec, s[0:1]
	s_waitcnt lgkmcnt(0)
	s_barrier
	s_cbranch_vccnz .LBB0_219
	v_readlane_b32 s0, v255, 18
	s_mulk_i32 s0, 0x2100
	v_lshrrev_b32_e32 v98, 3, v1
	v_and_b32_e32 v4, 7, v0
	s_add_i32 s0, s0, 0
	v_readlane_b32 s2, v255, 8
	v_mul_u32_u24_e32 v3, 0x84, v98
	v_lshlrev_b32_e32 v5, 4, v4
	s_cmpk_lt_u32 s10, 0x100
	s_mul_i32 s1, s2, s35
	v_add3_u32 v99, s0, v3, v5
	v_lshlrev_b32_e32 v102, 3, v4
	v_mul_u32_u24_e32 v3, 0x420, v4
	v_lshlrev_b32_e32 v4, 2, v98
	s_cselect_b64 s[80:81], -1, 0
	s_lshl_b32 s66, s1, 2
	v_mov_b32_e32 v101, 0
	v_lshlrev_b32_e32 v2, 2, v0
	v_add3_u32 v105, s0, v3, v4
	v_lshlrev_b32_e32 v100, 4, v1
	v_readlane_b32 s0, v255, 14
	v_and_b32_e32 v2, 28, v2
	v_lshl_add_u64 v[110:111], s[14:15], 0, v[100:101]
	global_load_dwordx4 v[134:137], v[110:111], off
	global_load_dwordx4 v[138:141], v[110:111], off offset:1024
	global_load_dwordx4 v[142:145], v[110:111], off offset:2048
	global_load_dwordx4 v[146:149], v[110:111], off offset:3072
	v_lshl_add_u64 v[112:113], s[12:13], 0, v[100:101]
	v_lshlrev_b32_e32 v100, 2, v1
	v_readlane_b32 s1, v255, 15
	s_add_u32 s82, s90, 0xe00400
	v_cmp_eq_u32_e64 s[6:7], 0, v1
	v_lshl_add_u64 v[114:115], s[0:1], 0, v[100:101]
	v_lshlrev_b32_e32 v100, 2, v2
	v_mbcnt_lo_u32_b32 v2, -1, 0
	s_mul_i32 s67, s33, s2
	s_addc_u32 s83, s91, 0
	v_mov_b32_e32 v103, v101
	v_or_b32_e32 v104, 8, v98
	v_or_b32_e32 v106, 16, v98
	v_or_b32_e32 v108, 24, v98
	s_add_i32 s90, 0, 0x20284
	s_add_i32 s91, 0, 0x20280
	v_mov_b32_e32 v107, 0x3727c5ac
	s_mov_b32 s92, 0xf800000
	v_mov_b32_e32 v109, 0x260
	v_mbcnt_hi_u32_b32 v116, -1, v2
	s_branch .LBB0_23

.LBB0_151:
	s_or_b64 exec, exec, s[0:1]
	v_readfirstlane_b32 s2, v2
	s_cmp_ge_i32 s2, s35
	s_mov_b64 s[0:1], 0
	s_cbranch_scc1 .LBB0_155
	s_lshl_b32 s0, s2, 2
	s_add_i32 s60, s0, s66
	s_cmpk_gt_i32 s60, 0x3fff
	s_cbranch_scc1 .LBB0_154
	s_ashr_i32 s61, s60, 31
	s_lshl_b64 s[0:1], s[60:61], 12
	v_lshl_add_u64 v[2:3], v[112:113], 0, s[0:1]
	global_load_dwordx4 v[42:45], v[2:3], off nt
	global_load_dwordx4 v[30:33], v[2:3], off offset:1024 nt
	global_load_dwordx4 v[18:21], v[2:3], off offset:2048 nt
	global_load_dwordx4 v[6:9], v[2:3], off offset:3072 nt
	s_or_b32 s28, s60, 1
	s_ashr_i32 s29, s28, 31
	s_lshl_b64 s[0:1], s[28:29], 12
	v_lshl_add_u64 v[2:3], v[112:113], 0, s[0:1]
	global_load_dwordx4 v[38:41], v[2:3], off nt
	global_load_dwordx4 v[26:29], v[2:3], off offset:1024 nt
	global_load_dwordx4 v[14:17], v[2:3], off offset:2048 nt
	s_nop 0
	global_load_dwordx4 v[2:5], v[2:3], off offset:3072 nt
	s_waitcnt vmcnt(28)
	v_and_b32_e32 v10, 64, v116
	v_xor_b32_e32 v11, 1, v116
	s_waitcnt vmcnt(18)
	v_add_u32_e32 v52, 64, v10
	v_xor_b32_e32 v12, 2, v116
	v_cmp_lt_i32_e32 vcc, v11, v52
	s_or_b32 s14, s60, 2
	v_xor_b32_e32 v13, 4, v116
	v_cndmask_b32_e32 v23, v116, v11, vcc
	v_cmp_lt_i32_e32 vcc, v12, v52
	v_xor_b32_e32 v22, 8, v116
	s_ashr_i32 s15, s14, 31
	v_cndmask_b32_e32 v12, v116, v12, vcc
	v_cmp_lt_i32_e32 vcc, v13, v52
	s_lshl_b64 s[2:3], s[14:15], 12
	v_lshl_add_u64 v[10:11], v[112:113], 0, s[2:3]
	v_cndmask_b32_e32 v13, v116, v13, vcc
	v_cmp_lt_i32_e32 vcc, v22, v52
	s_waitcnt vmcnt(14)
	v_lshlrev_b32_e32 v69, 2, v23
	v_lshlrev_b32_e32 v68, 2, v12
	v_cndmask_b32_e32 v22, v116, v22, vcc
	v_lshlrev_b32_e32 v67, 2, v13
	v_lshlrev_b32_e32 v66, 2, v22
	global_load_dwordx4 v[46:49], v[10:11], off nt
	global_load_dwordx4 v[34:37], v[10:11], off offset:1024 nt
	global_load_dwordx4 v[22:25], v[10:11], off offset:2048 nt
	s_nop 0
	global_load_dwordx4 v[10:13], v[10:11], off offset:3072 nt
	v_xor_b32_e32 v50, 16, v116
	v_cmp_lt_i32_e32 vcc, v50, v52
	v_xor_b32_e32 v51, 32, v116
	s_or_b32 s0, s60, 3
	v_cndmask_b32_e32 v50, v116, v50, vcc
	s_waitcnt vmcnt(16)
	v_lshlrev_b32_e32 v74, 2, v50
	v_cmp_lt_i32_e32 vcc, v51, v52
	s_ashr_i32 s1, s0, 31
	s_lshl_b64 s[2:3], s[0:1], 12
	v_cndmask_b32_e32 v51, v116, v51, vcc
	v_lshlrev_b32_e32 v75, 2, v51
	s_lshl_b64 s[0:1], s[0:1], 10
	s_waitcnt vmcnt(11)
	v_mul_f32_e32 v53, v43, v43
	v_mul_f32_e32 v54, v45, v45
	s_waitcnt vmcnt(10)
	v_mul_f32_e32 v55, v31, v31
	v_mul_f32_e32 v56, v33, v33
	s_waitcnt vmcnt(9)
	v_mul_f32_e32 v57, v19, v19
	v_mul_f32_e32 v58, v21, v21
	v_fmac_f32_e32 v53, v42, v42
	v_fmac_f32_e32 v54, v44, v44
	v_fmac_f32_e32 v55, v30, v30
	v_fmac_f32_e32 v56, v32, v32
	s_waitcnt vmcnt(8)
	v_mul_f32_e32 v59, v7, v7
	v_mul_f32_e32 v60, v9, v9
	v_fmac_f32_e32 v57, v18, v18
	v_fmac_f32_e32 v58, v20, v20
	v_add_f32_e32 v53, v53, v54
	v_add_f32_e32 v54, v55, v56
	v_fmac_f32_e32 v59, v6, v6
	v_fmac_f32_e32 v60, v8, v8
	v_add_f32_e32 v55, v57, v58
	v_add_f32_e32 v53, v53, v54
	v_add_f32_e32 v56, v59, v60
	v_add_f32_e32 v53, v53, v55
	v_add_f32_e32 v53, v53, v56
	ds_bpermute_b32 v54, v69, v53
	s_waitcnt vmcnt(7)
	v_mul_f32_e32 v61, v39, v39
	v_mul_f32_e32 v62, v41, v41
	s_waitcnt vmcnt(6)
	v_mul_f32_e32 v63, v27, v27
	v_mul_f32_e32 v64, v29, v29
	s_waitcnt lgkmcnt(0)
	v_add_f32_e32 v53, v53, v54
	ds_bpermute_b32 v54, v68, v53
	s_waitcnt vmcnt(5)
	v_mul_f32_e32 v65, v15, v15
	v_mul_f32_e32 v70, v17, v17
	v_fmac_f32_e32 v61, v38, v38
	v_fmac_f32_e32 v62, v40, v40
	s_waitcnt lgkmcnt(0)
	v_add_f32_e32 v53, v53, v54
	ds_bpermute_b32 v54, v67, v53
	v_fmac_f32_e32 v63, v26, v26
	v_fmac_f32_e32 v64, v28, v28
	s_waitcnt vmcnt(4)
	v_mul_f32_e32 v71, v3, v3
	v_mul_f32_e32 v72, v5, v5
	v_fmac_f32_e32 v65, v14, v14
	v_fmac_f32_e32 v70, v16, v16
	v_add_f32_e32 v55, v61, v62
	v_add_f32_e32 v56, v63, v64
	v_fmac_f32_e32 v71, v2, v2
	v_fmac_f32_e32 v72, v4, v4
	v_add_f32_e32 v57, v65, v70
	v_add_f32_e32 v55, v55, v56
	s_waitcnt lgkmcnt(0)
	v_add_f32_e32 v53, v53, v54
	v_add_f32_e32 v58, v71, v72
	v_add_f32_e32 v55, v55, v57
	ds_bpermute_b32 v54, v66, v53
	v_add_f32_e32 v55, v55, v58
	ds_bpermute_b32 v56, v69, v55
	s_waitcnt vmcnt(3)
	v_mul_f32_e32 v80, v47, v47
	v_mul_f32_e32 v81, v49, v49
	s_waitcnt lgkmcnt(1)
	v_add_f32_e32 v53, v53, v54
	ds_bpermute_b32 v54, v74, v53
	s_waitcnt lgkmcnt(1)
	v_add_f32_e32 v50, v55, v56
	ds_bpermute_b32 v55, v68, v50
	v_fmac_f32_e32 v80, v46, v46
	v_fmac_f32_e32 v81, v48, v48
	s_waitcnt lgkmcnt(1)
	v_add_f32_e32 v53, v53, v54
	ds_bpermute_b32 v54, v75, v53
	s_waitcnt lgkmcnt(1)
	v_add_f32_e32 v52, v50, v55
	ds_bpermute_b32 v55, v67, v52
	v_lshl_add_u64 v[50:51], v[112:113], 0, s[2:3]
	global_load_dwordx4 v[62:65], v[50:51], off nt
	global_load_dwordx4 v[58:61], v[50:51], off offset:1024 nt
	s_waitcnt lgkmcnt(1)
	v_add_f32_e32 v53, v53, v54
	v_fmamk_f32 v53, v53, 0x3a800000, v107
	s_waitcnt lgkmcnt(0)
	v_add_f32_e32 v52, v52, v55
	v_mul_f32_e32 v54, 0x4f800000, v53
	v_cmp_gt_f32_e32 vcc, s92, v53
	ds_bpermute_b32 v55, v66, v52
	v_add_f32_e32 v80, v80, v81
	v_cndmask_b32_e32 v53, v53, v54, vcc
	v_sqrt_f32_e32 v54, v53
	s_waitcnt vmcnt(4)
	v_mul_f32_e32 v81, v35, v35
	s_waitcnt lgkmcnt(0)
	v_add_f32_e32 v70, v52, v55
	v_mul_f32_e32 v82, v37, v37
	v_add_u32_e32 v52, -1, v54
	v_add_u32_e32 v55, 1, v54
	v_fma_f32 v56, -v52, v54, v53
	v_fma_f32 v57, -v55, v54, v53
	v_cmp_ge_f32_e64 s[4:5], 0, v56
	ds_bpermute_b32 v76, v74, v70
	v_fmac_f32_e32 v81, v34, v34
	v_cndmask_b32_e64 v52, v54, v52, s[4:5]
	v_cmp_lt_f32_e64 s[4:5], 0, v57
	v_fmac_f32_e32 v82, v36, v36
	v_add_f32_e32 v81, v81, v82
	v_cndmask_b32_e64 v52, v52, v55, s[4:5]
	v_mul_f32_e32 v54, 0x37800000, v52
	v_cndmask_b32_e32 v52, v52, v54, vcc
	v_cmp_class_f32_e32 vcc, v53, v109
	v_add_f32_e32 v80, v80, v81
	s_waitcnt vmcnt(3)
	v_mul_f32_e32 v81, v23, v23
	v_cndmask_b32_e32 v71, v52, v53, vcc
	global_load_dwordx4 v[54:57], v[50:51], off offset:2048 nt
	s_nop 0
	global_load_dwordx4 v[50:53], v[50:51], off offset:3072 nt
	v_mul_f32_e32 v82, v25, v25
	v_fmac_f32_e32 v81, v22, v22
	v_fmac_f32_e32 v82, v24, v24
	v_add_f32_e32 v81, v81, v82
	s_waitcnt lgkmcnt(0)
	v_add_f32_e32 v70, v70, v76
	v_add_f32_e32 v80, v80, v81
	s_waitcnt vmcnt(4)
	v_mul_f32_e32 v81, v11, v11
	v_mul_f32_e32 v82, v13, v13
	ds_bpermute_b32 v76, v75, v70
	v_fmac_f32_e32 v81, v10, v10
	v_fmac_f32_e32 v82, v12, v12
	v_add_f32_e32 v81, v81, v82
	v_add_f32_e32 v80, v80, v81
	v_div_scale_f32 v72, s[2:3], v71, v71, 1.0
	ds_bpermute_b32 v81, v69, v80
	v_rcp_f32_e32 v73, v72
	s_waitcnt lgkmcnt(1)
	v_add_f32_e32 v70, v70, v76
	v_fmamk_f32 v70, v70, 0x3a800000, v107
	v_mul_f32_e32 v76, 0x4f800000, v70
	v_cmp_gt_f32_e64 s[4:5], s92, v70
	v_fma_f32 v77, -v72, v73, 1.0
	s_waitcnt lgkmcnt(0)
	v_add_f32_e32 v80, v80, v81
	v_cndmask_b32_e64 v70, v70, v76, s[4:5]
	v_fmac_f32_e32 v73, v77, v73
	v_div_scale_f32 v77, vcc, 1.0, v71, 1.0
	v_sqrt_f32_e32 v76, v70
	ds_bpermute_b32 v81, v68, v80
	v_mul_f32_e32 v78, v77, v73
	v_fma_f32 v79, -v72, v78, v77
	v_fmac_f32_e32 v78, v79, v73
	v_fma_f32 v72, -v72, v78, v77
	v_add_u32_e32 v77, -1, v76
	v_fma_f32 v79, -v77, v76, v70
	s_waitcnt lgkmcnt(0)
	v_add_f32_e32 v80, v80, v81
	v_cmp_ge_f32_e64 s[8:9], 0, v79
	v_add_u32_e32 v79, 1, v76
	ds_bpermute_b32 v81, v67, v80
	v_cndmask_b32_e64 v77, v76, v77, s[8:9]
	v_fma_f32 v76, -v79, v76, v70
	v_cmp_lt_f32_e64 s[8:9], 0, v76
	v_div_fmas_f32 v72, v72, v73, v78
	v_div_fixup_f32 v78, v72, v71, 1.0
	v_cndmask_b32_e64 v76, v77, v79, s[8:9]
	v_mul_f32_e32 v77, 0x37800000, v76
	v_cndmask_b32_e64 v76, v76, v77, s[4:5]
	s_waitcnt lgkmcnt(0)
	v_add_f32_e32 v77, v80, v81
	ds_bpermute_b32 v79, v66, v77
	v_cmp_class_f32_e64 s[4:5], v70, v109
	s_waitcnt vmcnt(2)
	v_mul_f32_e32 v72, v61, v61
	v_fmac_f32_e32 v72, v60, v60
	v_cndmask_b32_e64 v76, v76, v70, s[4:5]
	s_waitcnt lgkmcnt(0)
	v_add_f32_e32 v70, v77, v79
	v_div_scale_f32 v80, s[2:3], v76, v76, 1.0
	ds_bpermute_b32 v77, v74, v70
	v_rcp_f32_e32 v81, v80
	v_mul_f32_e32 v42, v42, v78
	v_mul_f32_e32 v43, v43, v78
	v_mul_f32_e32 v44, v44, v78
	v_fma_f32 v71, -v80, v81, 1.0
	s_waitcnt lgkmcnt(0)
	v_add_f32_e32 v70, v70, v77
	v_fmac_f32_e32 v81, v71, v81
	ds_bpermute_b32 v71, v75, v70
	v_div_scale_f32 v77, vcc, 1.0, v76, 1.0
	v_mul_f32_e32 v79, v77, v81
	v_fma_f32 v82, -v80, v79, v77
	s_waitcnt lgkmcnt(0)
	v_add_f32_e32 v70, v70, v71
	v_fmamk_f32 v70, v70, 0x3a800000, v107
	v_mul_f32_e32 v71, 0x4f800000, v70
	v_cmp_gt_f32_e64 s[4:5], s92, v70
	v_fmac_f32_e32 v79, v82, v81
	v_fma_f32 v77, -v80, v79, v77
	v_cndmask_b32_e64 v83, v70, v71, s[4:5]
	v_mul_f32_e32 v70, v63, v63
	v_mul_f32_e32 v71, v65, v65
	v_fmac_f32_e32 v70, v62, v62
	v_fmac_f32_e32 v71, v64, v64
	v_add_f32_e32 v70, v70, v71
	v_mul_f32_e32 v71, v59, v59
	v_fmac_f32_e32 v71, v58, v58
	v_add_f32_e32 v71, v71, v72
	v_add_f32_e32 v70, v70, v71
	s_waitcnt vmcnt(1)
	v_mul_f32_e32 v71, v55, v55
	v_mul_f32_e32 v72, v57, v57
	v_fmac_f32_e32 v71, v54, v54
	v_fmac_f32_e32 v72, v56, v56
	v_add_f32_e32 v71, v71, v72
	v_add_f32_e32 v85, v70, v71
	s_waitcnt vmcnt(0)
	v_mul_f32_e32 v86, v51, v51
	v_mul_f32_e32 v87, v53, v53
	v_fmac_f32_e32 v86, v50, v50
	v_fmac_f32_e32 v87, v52, v52
	v_add_f32_e32 v86, v86, v87
	v_add_f32_e32 v85, v85, v86
	ds_bpermute_b32 v69, v69, v85
	v_sqrt_f32_e32 v84, v83
	v_mul_f32_e32 v30, v30, v78
	v_mul_f32_e32 v31, v31, v78
	v_mul_f32_e32 v32, v32, v78
	s_waitcnt lgkmcnt(0)
	v_add_f32_e32 v69, v85, v69
	ds_bpermute_b32 v68, v68, v69
	v_add_u32_e32 v80, -1, v84
	v_fma_f32 v82, -v80, v84, v83
	v_cmp_ge_f32_e64 s[8:9], 0, v82
	v_add_u32_e32 v82, 1, v84
	s_waitcnt lgkmcnt(0)
	v_add_f32_e32 v68, v69, v68
	ds_bpermute_b32 v67, v67, v68
	v_cndmask_b32_e64 v80, v84, v80, s[8:9]
	v_fma_f32 v84, -v82, v84, v83
	v_cmp_lt_f32_e64 s[8:9], 0, v84
	v_mul_f32_e32 v18, v18, v78
	s_waitcnt lgkmcnt(0)
	v_add_f32_e32 v67, v68, v67
	ds_bpermute_b32 v66, v66, v67
	v_cndmask_b32_e64 v69, v80, v82, s[8:9]
	v_mul_f32_e32 v80, 0x37800000, v69
	v_cndmask_b32_e64 v69, v69, v80, s[4:5]
	v_cmp_class_f32_e64 s[4:5], v83, v109
	s_waitcnt lgkmcnt(0)
	v_add_f32_e32 v66, v67, v66
	ds_bpermute_b32 v67, v74, v66
	v_cndmask_b32_e64 v68, v69, v83, s[4:5]
	v_div_scale_f32 v69, s[2:3], v68, v68, 1.0
	v_rcp_f32_e32 v80, v69
	s_waitcnt lgkmcnt(0)
	v_add_f32_e32 v66, v66, v67
	ds_bpermute_b32 v67, v75, v66
	v_div_fmas_f32 v74, v77, v81, v79
	v_div_fixup_f32 v74, v74, v76, 1.0
	v_fma_f32 v76, -v69, v80, 1.0
	v_fmac_f32_e32 v80, v76, v80
	s_waitcnt lgkmcnt(0)
	v_add_f32_e32 v66, v66, v67
	v_fmamk_f32 v66, v66, 0x3a800000, v107
	v_mul_f32_e32 v67, 0x4f800000, v66
	v_cmp_gt_f32_e64 s[4:5], s92, v66
	v_div_scale_f32 v75, vcc, 1.0, v68, 1.0
	s_nop 0
	v_cndmask_b32_e64 v66, v66, v67, s[4:5]
	v_sqrt_f32_e32 v67, v66
	v_mul_f32_e32 v76, v75, v80
	v_fma_f32 v77, -v69, v76, v75
	v_fmac_f32_e32 v76, v77, v80
	v_fma_f32 v69, -v69, v76, v75
	v_add_u32_e32 v75, -1, v67
	v_fma_f32 v77, -v75, v67, v66
	v_cmp_ge_f32_e64 s[8:9], 0, v77
	v_add_u32_e32 v77, 1, v67
	v_div_fmas_f32 v69, v69, v80, v76
	v_cndmask_b32_e64 v75, v67, v75, s[8:9]
	v_fma_f32 v67, -v77, v67, v66
	v_cmp_lt_f32_e64 s[8:9], 0, v67
	v_div_fixup_f32 v68, v69, v68, 1.0
	v_mul_f32_e32 v38, v38, v74
	v_cndmask_b32_e64 v67, v75, v77, s[8:9]
	v_mul_f32_e32 v75, 0x37800000, v67
	v_cndmask_b32_e64 v67, v67, v75, s[4:5]
	v_cmp_class_f32_e64 s[4:5], v66, v109
	v_mul_f32_e32 v39, v39, v74
	v_mul_f32_e32 v40, v40, v74
	v_cndmask_b32_e64 v66, v67, v66, s[4:5]
	v_div_scale_f32 v67, s[2:3], v66, v66, 1.0
	v_rcp_f32_e32 v75, v67
	s_lshl_b64 s[2:3], s[60:61], 10
	v_mul_f32_e32 v26, v26, v74
	v_mul_f32_e32 v27, v27, v74
	v_fma_f32 v69, -v67, v75, 1.0
	v_fmac_f32_e32 v75, v69, v75
	v_div_scale_f32 v69, vcc, 1.0, v66, 1.0
	v_mul_f32_e32 v76, v69, v75
	v_fma_f32 v77, -v67, v76, v69
	v_fmac_f32_e32 v76, v77, v75
	v_fma_f32 v67, -v67, v76, v69
	s_waitcnt vmcnt(0)
	v_mul_f32_e32 v38, v38, v134
	v_mul_f32_e32 v39, v39, v135
	v_mov_b32_e32 v69, v101
	v_cvt_pk_fp8_f32 v69, v38, v39
	v_mul_f32_e32 v39, v41, v74
	v_mul_f32_e32 v38, v40, v136
	v_mul_f32_e32 v39, v39, v137
	v_cvt_pk_fp8_f32 v69, v38, v39 op_sel:[0,0,1]
	v_mul_f32_e32 v38, v46, v68
	v_mul_f32_e32 v39, v47, v68
	v_mul_f32_e32 v38, v38, v134
	v_mul_f32_e32 v39, v39, v135
	v_mov_b32_e32 v41, v101
	v_cvt_pk_fp8_f32 v41, v38, v39
	v_div_fmas_f32 v67, v67, v75, v76
	v_mul_f32_e32 v40, v48, v68
	v_mul_f32_e32 v39, v49, v68
	v_div_fixup_f32 v66, v67, v66, 1.0
	v_mul_f32_e32 v38, v40, v136
	v_mul_f32_e32 v39, v39, v137
	v_cvt_pk_fp8_f32 v41, v38, v39 op_sel:[0,0,1]
	v_mul_f32_e32 v38, v62, v66
	v_mul_f32_e32 v39, v63, v66
	v_mul_f32_e32 v42, v42, v134
	v_mul_f32_e32 v43, v43, v135
	v_mov_b32_e32 v67, v101
	v_mul_f32_e32 v38, v134, v38
	v_mul_f32_e32 v39, v135, v39
	v_mov_b32_e32 v62, v101
	v_cvt_pk_fp8_f32 v67, v42, v43
	v_cvt_pk_fp8_f32 v62, v38, v39
	v_mul_f32_e32 v43, v45, v78
	v_mul_f32_e32 v40, v64, v66
	v_mul_f32_e32 v39, v65, v66
	v_mul_f32_e32 v42, v44, v136
	v_mul_f32_e32 v43, v43, v137
	v_mul_f32_e32 v38, v136, v40
	v_mul_f32_e32 v39, v137, v39
	v_cvt_pk_fp8_f32 v67, v42, v43 op_sel:[0,0,1]
	v_cvt_pk_fp8_f32 v62, v38, v39 op_sel:[0,0,1]
	v_lshl_add_u64 v[42:43], v[114:115], 0, s[2:3]
	s_lshl_b64 s[2:3], s[28:29], 10
	v_lshl_add_u64 v[44:45], v[114:115], 0, s[2:3]
	s_lshl_b64 s[2:3], s[14:15], 10
	v_lshl_add_u64 v[46:47], v[114:115], 0, s[2:3]
	v_lshl_add_u64 v[48:49], v[114:115], 0, s[0:1]
	global_store_dword v[42:43], v67, off
	global_store_dword v[44:45], v69, off
	global_store_dword v[46:47], v41, off
	global_store_dword v[48:49], v62, off
	v_mov_b32_e32 v62, v101
	v_mul_f32_e32 v28, v28, v74
	v_mul_f32_e32 v19, v19, v78
	v_mul_f32_e32 v20, v20, v78
	v_mul_f32_e32 v14, v14, v74
	v_mul_f32_e32 v15, v15, v74
	v_mul_f32_e32 v16, v16, v74
	v_mul_f32_e32 v6, v6, v78
	v_mul_f32_e32 v7, v7, v78
	v_mul_f32_e32 v8, v8, v78
	v_mul_f32_e32 v2, v2, v74
	v_mul_f32_e32 v3, v3, v74
	v_mul_f32_e32 v4, v4, v74
	v_mul_f32_e32 v30, v30, v138
	v_mul_f32_e32 v31, v31, v139
	v_cvt_pk_fp8_f32 v62, v30, v31
	v_mul_f32_e32 v31, v33, v78
	v_mul_f32_e32 v30, v32, v140
	v_mul_f32_e32 v31, v31, v141
	v_cvt_pk_fp8_f32 v62, v30, v31 op_sel:[0,0,1]
	v_mul_f32_e32 v26, v26, v138
	v_mul_f32_e32 v27, v27, v139
	v_mov_b32_e32 v30, v101
	v_cvt_pk_fp8_f32 v30, v26, v27
	v_mul_f32_e32 v27, v29, v74
	v_mul_f32_e32 v26, v28, v140
	v_mul_f32_e32 v27, v27, v141
	v_cvt_pk_fp8_f32 v30, v26, v27 op_sel:[0,0,1]
	v_mul_f32_e32 v26, v34, v68
	v_mul_f32_e32 v27, v35, v68
	v_mul_f32_e32 v26, v26, v138
	v_mul_f32_e32 v27, v27, v139
	v_mov_b32_e32 v29, v101
	v_cvt_pk_fp8_f32 v29, v26, v27
	v_mul_f32_e32 v28, v36, v68
	v_mul_f32_e32 v27, v37, v68
	v_mul_f32_e32 v26, v28, v140
	v_mul_f32_e32 v27, v27, v141
	v_cvt_pk_fp8_f32 v29, v26, v27 op_sel:[0,0,1]
	v_mul_f32_e32 v26, v58, v66
	v_mul_f32_e32 v27, v59, v66
	v_mul_f32_e32 v26, v26, v138
	v_mul_f32_e32 v27, v27, v139
	v_mov_b32_e32 v31, v101
	v_cvt_pk_fp8_f32 v31, v26, v27
	v_mul_f32_e32 v28, v60, v66
	v_mul_f32_e32 v27, v61, v66
	v_mul_f32_e32 v26, v28, v140
	v_mul_f32_e32 v27, v27, v141
	v_cvt_pk_fp8_f32 v31, v26, v27 op_sel:[0,0,1]
	global_store_dword v[42:43], v62, off offset:256
	global_store_dword v[44:45], v30, off offset:256
	global_store_dword v[46:47], v29, off offset:256
	global_store_dword v[48:49], v31, off offset:256
	v_mov_b32_e32 v30, v101
	v_mul_f32_e32 v18, v18, v142
	v_mul_f32_e32 v19, v19, v143
	v_cvt_pk_fp8_f32 v30, v18, v19
	v_mul_f32_e32 v19, v21, v78
	v_mul_f32_e32 v18, v20, v144
	v_mul_f32_e32 v19, v19, v145
	v_cvt_pk_fp8_f32 v30, v18, v19 op_sel:[0,0,1]
	v_mul_f32_e32 v14, v14, v142
	v_mul_f32_e32 v15, v15, v143
	v_mov_b32_e32 v18, v101
	v_cvt_pk_fp8_f32 v18, v14, v15
	v_mul_f32_e32 v15, v17, v74
	v_mul_f32_e32 v14, v16, v144
	v_mul_f32_e32 v15, v15, v145
	v_cvt_pk_fp8_f32 v18, v14, v15 op_sel:[0,0,1]
	v_mul_f32_e32 v14, v22, v68
	v_mul_f32_e32 v15, v23, v68
	v_mul_f32_e32 v14, v14, v142
	v_mul_f32_e32 v15, v15, v143
	v_mov_b32_e32 v17, v101
	v_cvt_pk_fp8_f32 v17, v14, v15
	v_mul_f32_e32 v16, v24, v68
	v_mul_f32_e32 v15, v25, v68
	v_mul_f32_e32 v14, v16, v144
	v_mul_f32_e32 v15, v15, v145
	v_cvt_pk_fp8_f32 v17, v14, v15 op_sel:[0,0,1]
	v_mul_f32_e32 v14, v54, v66
	v_mul_f32_e32 v15, v55, v66
	v_mul_f32_e32 v14, v14, v142
	v_mul_f32_e32 v15, v15, v143
	v_mov_b32_e32 v19, v101
	v_cvt_pk_fp8_f32 v19, v14, v15
	v_mul_f32_e32 v16, v56, v66
	v_mul_f32_e32 v15, v57, v66
	v_mul_f32_e32 v14, v16, v144
	v_mul_f32_e32 v15, v15, v145
	v_cvt_pk_fp8_f32 v19, v14, v15 op_sel:[0,0,1]
	global_store_dword v[42:43], v30, off offset:512
	global_store_dword v[44:45], v18, off offset:512
	global_store_dword v[46:47], v17, off offset:512
	global_store_dword v[48:49], v19, off offset:512
	v_mov_b32_e32 v18, v101
	v_mul_f32_e32 v6, v6, v146
	v_mul_f32_e32 v7, v7, v147
	v_cvt_pk_fp8_f32 v18, v6, v7
	v_mul_f32_e32 v7, v9, v78
	v_mul_f32_e32 v6, v8, v148
	v_mul_f32_e32 v7, v7, v149
	v_cvt_pk_fp8_f32 v18, v6, v7 op_sel:[0,0,1]
	v_mul_f32_e32 v2, v2, v146
	v_mul_f32_e32 v3, v3, v147
	v_mov_b32_e32 v6, v101
	v_cvt_pk_fp8_f32 v6, v2, v3
	v_mul_f32_e32 v3, v5, v74
	v_mul_f32_e32 v2, v4, v148
	v_mul_f32_e32 v3, v3, v149
	v_cvt_pk_fp8_f32 v6, v2, v3 op_sel:[0,0,1]
	v_mul_f32_e32 v2, v10, v68
	v_mul_f32_e32 v3, v11, v68
	v_mul_f32_e32 v2, v2, v146
	v_mul_f32_e32 v3, v3, v147
	v_mov_b32_e32 v5, v101
	v_cvt_pk_fp8_f32 v5, v2, v3
	v_mul_f32_e32 v4, v12, v68
	v_mul_f32_e32 v3, v13, v68
	v_mul_f32_e32 v2, v4, v148
	v_mul_f32_e32 v3, v3, v149
	v_cvt_pk_fp8_f32 v5, v2, v3 op_sel:[0,0,1]
	v_mul_f32_e32 v2, v50, v66
	v_mul_f32_e32 v3, v51, v66
	v_mul_f32_e32 v2, v2, v146
	v_mul_f32_e32 v3, v3, v147
	v_mov_b32_e32 v7, v101
	v_cvt_pk_fp8_f32 v7, v2, v3
	v_mul_f32_e32 v4, v52, v66
	v_mul_f32_e32 v3, v53, v66
	v_mul_f32_e32 v2, v4, v148
	v_mul_f32_e32 v3, v3, v149
	v_cvt_pk_fp8_f32 v7, v2, v3 op_sel:[0,0,1]
	global_store_dword v[42:43], v18, off offset:768
	global_store_dword v[44:45], v6, off offset:768
	global_store_dword v[46:47], v5, off offset:768
	global_store_dword v[48:49], v7, off offset:768
